# norm2 row loop: the weight/shift/scale loads of column groups 1-3 are issued up front with the first group and consumed with counted waits (was one load/full-wait round trip per column group); plus pr
# baseline (speedup 1.0000x reference)
;     __device__ __forceinline__ float* mods() const { return (float*)(ws + WS_MODS); }
; __device__ __forceinline__ void phase_norm2_route(const Frame& F, const Params& P, int l, int nrows, long long dctx) {
;     ...
;     for (int rowA = r0 + F.wid; rowA < r1; rowA += 16) {
;         const int rowB = rowA + 8; const bool hasB = rowB < r1; const int rowBs = hasB ? rowB : rowA;
;         const float* xa = xrow_ptr(P.out, dctx, rowA); const float* xb = xrow_ptr(P.out, dctx, rowBs);
;         f32x4 va[4], vb[4]; float sa = 0.f, sb = 0.f;
; #pragma unroll
;         for (int j = 0; j < 4; ++j) { va[j] = *(const f32x4*)(xa + F.lane * 4 + 256 * j); vb[j] = *(const f32x4*)(xb + F.lane * 4 + 256 * j); }
; #pragma unroll
;         for (int j = 0; j < 4; ++j) { sa += va[j][0] * va[j][0] + va[j][1] * va[j][1] + va[j][2] * va[j][2] + va[j][3] * va[j][3]; sb += vb[j][0] * vb[j][0] + vb[j][1] * vb[j][1] + vb[j][2] * vb[j][2] + vb[j][3] * vb[j][3]; }
;         sa = wave_sum(sa); sb = wave_sum(sb);
;         const float ra = rsqrtf(sa * (1.f / 1024.f) + EPS), rb = rsqrtf(sb * (1.f / 1024.f) + EPS);
;         const float* mda = F.mods() + (size_t)(l * 9 + (rowA < TL ? (rowA >> 13) : 8)) * 6144;
;         const float* mdb = F.mods() + (size_t)(l * 9 + (rowBs < TL ? (rowBs >> 13) : 8)) * 6144;
; #pragma unroll
;         for (int j = 0; j < 4; ++j) {
;             const int col = F.lane * 4 + 256 * j;
;             const f32x4 gg = *(const f32x4*)(g + col);
;             const f32x4 sha = *(const f32x4*)(mda + 3 * 1024 + col), sca = *(const f32x4*)(mda + 4 * 1024 + col);
;             const f32x4 shb = *(const f32x4*)(mdb + 3 * 1024 + col), scb = *(const f32x4*)(mdb + 4 * 1024 + col);
;             float oa[4], ob[4];
; #pragma unroll
;             for (int i = 0; i < 4; ++i) { oa[i] = va[j][i] * ra * gg[i] * (1.f + sca[i]) + sha[i]; ob[i] = vb[j][i] * rb * gg[i] * (1.f + scb[i]) + shb[i]; }
.LBB0_925:
	s_add_i32 s18, s0, 8
	s_cmp_lt_i32 s18, s85
	s_cselect_b64 s[28:29], -1, 0
	s_and_b64 s[8:9], s[28:29], exec
	s_cselect_b32 s8, s18, s0
	s_cmp_gt_i32 s0, 0xffff
	s_cselect_b32 s22, s60, 0
	s_cselect_b32 s23, s61, 0
	s_ashr_i32 s9, s8, 31
	v_lshl_add_u64 v[2:3], s[22:23], 2, v[34:35]
	s_lshl_b64 s[22:23], s[8:9], 12
	global_load_dwordx4 v[26:29], v[2:3], off
	global_load_dwordx4 v[22:25], v[2:3], off offset:1024
	global_load_dwordx4 v[14:17], v[2:3], off offset:2048
	s_nop 0
	global_load_dwordx4 v[2:5], v[2:3], off offset:3072
	s_add_u32 s9, s36, s22
	s_addc_u32 s19, s37, s23
	s_cmp_gt_i32 s8, 0xffff
	s_cselect_b32 s23, s61, 0
	s_cselect_b32 s22, s60, 0
	s_lshl_b64 s[22:23], s[22:23], 2
	s_add_u32 s22, s9, s22
	s_addc_u32 s23, s19, s23
	global_load_dwordx4 v[44:47], v1, s[22:23]
	global_load_dwordx4 v[18:21], v1, s[22:23] offset:1024
	global_load_dwordx4 v[10:13], v1, s[22:23] offset:2048
	global_load_dwordx4 v[6:9], v1, s[22:23] offset:3072
	global_load_dwordx4 v[48:51], v[32:33], off
	s_min_i32 s9, s0, 0x10000
	s_ashr_i32 s9, s9, 13
	s_add_i32 s9, s9, s1
	s_mul_hi_i32 s19, s9, 0x6000
	s_mulk_i32 s9, 0x6000
	s_add_u32 s9, s2, s9
	s_addc_u32 s19, s7, s19
	s_min_i32 s8, s8, 0x10000
	s_ashr_i32 s8, s8, 13
	s_add_i32 s8, s8, s1
	s_mul_hi_i32 s22, s8, 0x6000
	s_mulk_i32 s8, 0x6000
	s_add_u32 s8, s2, s8
	s_addc_u32 s22, s7, s22
	s_add_u32 s48, s9, 0x3000
	s_addc_u32 s49, s19, 0
	s_add_u32 s52, s9, 0x4000
	s_addc_u32 s53, s19, 0
	s_add_u32 s50, s8, 0x3000
	global_load_dwordx4 v[52:55], v1, s[48:49]
	global_load_dwordx4 v[56:59], v1, s[52:53]
	s_addc_u32 s51, s22, 0
	s_add_u32 s54, s8, 0x4000
	s_addc_u32 s55, s22, 0
	global_load_dwordx4 v[60:63], v1, s[50:51]
	global_load_dwordx4 v[64:67], v1, s[54:55]
	s_mov_b32 s8, 0x3a800000
	s_cmp_ge_i32 s18, s85
	global_load_dwordx4 v[68:71], v[32:33], off offset:1024
	global_load_dwordx4 v[72:75], v38, s[48:49]
	global_load_dwordx4 v[76:79], v38, s[52:53]
	global_load_dwordx4 v[80:83], v38, s[50:51]
	global_load_dwordx4 v[84:87], v38, s[54:55]
	global_load_dwordx4 v[88:91], v[32:33], off offset:2048
	global_load_dwordx4 v[92:95], v39, s[48:49]
	global_load_dwordx4 v[96:99], v39, s[52:53]
	global_load_dwordx4 v[100:103], v39, s[50:51]
	global_load_dwordx4 v[104:107], v39, s[54:55]
	global_load_dwordx4 v[108:111], v[32:33], off offset:3072
	global_load_dwordx4 v[112:115], v40, s[52:53]
	global_load_dwordx4 v[116:119], v40, s[54:55]
	global_load_dwordx4 v[120:123], v40, s[48:49]
	global_load_dwordx4 v[124:127], v40, s[50:51]
	s_waitcnt vmcnt(15)
	v_mul_f32_e32 v36, v27, v27
	v_mul_f32_e32 v37, v23, v23
	v_mul_f32_e32 v41, v15, v15
	v_fmac_f32_e32 v36, v26, v26
	v_fmac_f32_e32 v37, v22, v22
	v_mul_f32_e32 v42, v3, v3
	v_fmac_f32_e32 v41, v14, v14
	v_fmac_f32_e32 v36, v28, v28
	v_fmac_f32_e32 v37, v24, v24
	v_fmac_f32_e32 v42, v2, v2
	v_fmac_f32_e32 v41, v16, v16
	v_fmac_f32_e32 v36, v29, v29
	v_fmac_f32_e32 v37, v25, v25
	v_fmac_f32_e32 v42, v4, v4
	v_fmac_f32_e32 v41, v17, v17
	v_add_f32_e32 v36, v36, v37
	v_fmac_f32_e32 v42, v5, v5
	v_add_f32_e32 v36, v36, v41
	v_add_f32_e32 v36, v36, v42
	v_mul_f32_e32 v37, v45, v45
	v_mul_f32_e32 v41, v19, v19
	v_mul_f32_e32 v42, v11, v11
	v_add_f32_dpp v36, v36, v36 quad_perm:[1,0,3,2] row_mask:0xf bank_mask:0xf bound_ctrl:1
	v_fmac_f32_e32 v37, v44, v44
	v_fmac_f32_e32 v41, v18, v18
	v_mul_f32_e32 v43, v7, v7
	v_fmac_f32_e32 v42, v10, v10
	v_add_f32_dpp v36, v36, v36 quad_perm:[2,3,0,1] row_mask:0xf bank_mask:0xf bound_ctrl:1
	v_fmac_f32_e32 v37, v46, v46
	v_fmac_f32_e32 v41, v20, v20
	v_fmac_f32_e32 v43, v6, v6
	v_fmac_f32_e32 v42, v12, v12
	v_add_f32_dpp v36, v36, v36 row_half_mirror row_mask:0xf bank_mask:0xf bound_ctrl:1
	v_fmac_f32_e32 v37, v47, v47
	v_fmac_f32_e32 v41, v21, v21
	v_fmac_f32_e32 v43, v8, v8
	v_fmac_f32_e32 v42, v13, v13
	v_add_f32_dpp v36, v36, v36 row_mirror row_mask:0xf bank_mask:0xf bound_ctrl:1
	v_add_f32_e32 v37, v37, v41
	v_fmac_f32_e32 v43, v9, v9
	v_mov_b32_e32 v41, v36
	v_add_f32_e32 v37, v37, v42
	s_nop 0
	v_permlane16_swap_b32_e32 v36, v41
	v_add_f32_e32 v42, v37, v43
	v_add_f32_e32 v37, v36, v41
	v_mov_b32_e32 v43, v37
	v_add_f32_dpp v36, v42, v42 quad_perm:[1,0,3,2] row_mask:0xf bank_mask:0xf bound_ctrl:1
	s_nop 0
	v_permlane32_swap_b32_e32 v37, v43
	v_add_f32_dpp v36, v36, v36 quad_perm:[2,3,0,1] row_mask:0xf bank_mask:0xf bound_ctrl:1
	s_nop 1
	v_add_f32_dpp v36, v36, v36 row_half_mirror row_mask:0xf bank_mask:0xf bound_ctrl:1
	s_nop 1
	v_add_f32_dpp v36, v36, v36 row_mirror row_mask:0xf bank_mask:0xf bound_ctrl:1
	v_mov_b32_e32 v41, v36
	s_nop 1
	v_permlane16_swap_b32_e32 v36, v41
	v_add_f32_e32 v36, v36, v41
	v_mov_b32_e32 v42, v36
	s_nop 1
	v_permlane32_swap_b32_e32 v36, v42
	v_pk_add_f32 v[36:37], v[36:37], v[42:43]
	v_add_f32_e32 v43, 1.0, v65
	v_pk_fma_f32 v[36:37], v[36:37], s[8:9], v[196:197] op_sel_hi:[1,0,0]
	s_nop 0
	v_mul_f32_e32 v41, 0x4b800000, v37
	v_cmp_gt_f32_e32 vcc, s3, v37
	v_cmp_gt_f32_e64 s[42:43], s3, v36
	s_nop 0
	v_cndmask_b32_e32 v37, v37, v41, vcc
	v_rsq_f32_e32 v37, v37
	v_mul_f32_e32 v41, 0x4b800000, v36
	v_cndmask_b32_e64 v36, v36, v41, s[42:43]
	v_rsq_f32_e32 v36, v36
	v_mul_f32_e32 v41, 0x45800000, v37
	v_cndmask_b32_e32 v42, v37, v41, vcc
	v_mul_f32_e32 v26, v26, v42
	v_mul_f32_e32 v37, 0x45800000, v36
	v_cndmask_b32_e64 v41, v36, v37, s[42:43]
	v_mul_f32_e32 v26, v48, v26
	v_add_f32_e32 v36, 1.0, v56
	v_fma_f32 v26, v36, v26, v52
	v_mul_f32_e32 v36, v44, v41
	v_mul_f32_e32 v36, v48, v36
	v_add_f32_e32 v37, 1.0, v64
	v_mul_f32_e32 v27, v27, v42
	v_fma_f32 v36, v37, v36, v60
	v_mul_f32_e32 v27, v49, v27
	v_add_f32_e32 v37, 1.0, v57
	v_fma_f32 v27, v37, v27, v53
	v_mul_f32_e32 v37, v45, v41
; __device__ __forceinline__ unsigned cvt_pk_bf16(float lo, float hi) { unsigned r; asm volatile("v_cvt_pk_bf16_f32 %0, %1, %2" : "=v"(r) : "v"(lo), "v"(hi)); return r; }
; __device__ __forceinline__ float bf_lo(unsigned w) { return __uint_as_float(w << 16); }
; __device__ __forceinline__ float bf_hi(unsigned w) { return __uint_as_float(w & 0xffff0000u); }
;     __device__ __forceinline__ bf16_t* H() const { return (bf16_t*)(ws + WS_H); }
; __device__ __forceinline__ void phase_norm2_route(const Frame& F, const Params& P, int l, int nrows, long long dctx) {
;     ...
;         for (int j = 0; j < 4; ++j) {
;             const int col = F.lane * 4 + 256 * j;
;             const f32x4 gg = *(const f32x4*)(g + col);
;             const f32x4 sha = *(const f32x4*)(mda + 3 * 1024 + col), sca = *(const f32x4*)(mda + 4 * 1024 + col);
;             const f32x4 shb = *(const f32x4*)(mdb + 3 * 1024 + col), scb = *(const f32x4*)(mdb + 4 * 1024 + col);
;             float oa[4], ob[4];
; #pragma unroll
;             for (int i = 0; i < 4; ++i) { oa[i] = va[j][i] * ra * gg[i] * (1.f + sca[i]) + sha[i]; ob[i] = vb[j][i] * rb * gg[i] * (1.f + scb[i]) + shb[i]; }
;             u32x2 ha, hb, la, lb;
;             ha.x = cvt_pk_bf16(oa[0], oa[1]); ha.y = cvt_pk_bf16(oa[2], oa[3]); hb.x = cvt_pk_bf16(ob[0], ob[1]); hb.y = cvt_pk_bf16(ob[2], ob[3]);
;             la.x = cvt_pk_bf16(oa[0] - bf_lo(ha.x), oa[1] - bf_hi(ha.x)); la.y = cvt_pk_bf16(oa[2] - bf_lo(ha.y), oa[3] - bf_hi(ha.y));
;             lb.x = cvt_pk_bf16(ob[0] - bf_lo(hb.x), ob[1] - bf_hi(hb.x)); lb.y = cvt_pk_bf16(ob[2] - bf_lo(hb.y), ob[3] - bf_hi(hb.y));
;             *(u32x2*)(F.H() + (size_t)rowA * DM + col) = ha; *(u32x2*)(LO + (size_t)rowA * DM + col) = la;
;             if (hasB) { *(u32x2*)(F.H() + (size_t)rowB * DM + col) = hb; *(u32x2*)(LO + (size_t)rowB * DM + col) = lb; }
;         }
	v_mul_f32_e32 v37, v49, v37
	v_mul_f32_e32 v28, v28, v42
	v_fma_f32 v37, v43, v37, v61
	v_mul_f32_e32 v28, v50, v28
	v_add_f32_e32 v43, 1.0, v58
	v_fma_f32 v43, v43, v28, v54
	v_mul_f32_e32 v28, v46, v41
	v_mul_f32_e32 v28, v50, v28
	v_add_f32_e32 v44, 1.0, v66
	v_fma_f32 v48, v44, v28, v62
	v_mul_f32_e32 v28, v29, v42
	v_mul_f32_e32 v28, v51, v28
	v_add_f32_e32 v29, 1.0, v59
	v_cvt_pk_bf16_f32 v44, v26, v27
	v_fmac_f32_e32 v55, v29, v28
	v_lshlrev_b32_e32 v46, 16, v44
	v_mul_f32_e32 v28, v47, v41
	v_sub_f32_e32 v26, v26, v46
	v_and_b32_e32 v46, 0xffff0000, v44
	v_mul_f32_e32 v28, v51, v28
	v_add_f32_e32 v29, 1.0, v67
	v_sub_f32_e32 v27, v27, v46
	v_fmac_f32_e32 v63, v29, v28
	v_cvt_pk_bf16_f32 v45, v43, v55
	v_cvt_pk_bf16_f32 v28, v36, v37
	v_cvt_pk_bf16_f32 v29, v48, v63
	v_cvt_pk_bf16_f32 v46, v26, v27
	s_nop 0
	v_lshlrev_b32_e32 v26, 16, v45
	v_and_b32_e32 v27, 0xffff0000, v45
	v_sub_f32_e32 v26, v43, v26
	v_sub_f32_e32 v27, v55, v27
	v_cvt_pk_bf16_f32 v47, v26, v27
	v_lshlrev_b32_e32 v26, 16, v28
	v_and_b32_e32 v27, 0xffff0000, v28
	v_sub_f32_e32 v26, v36, v26
	v_sub_f32_e32 v27, v37, v27
	v_cvt_pk_bf16_f32 v36, v26, v27
	v_lshlrev_b32_e32 v26, 16, v29
	v_and_b32_e32 v27, 0xffff0000, v29
	v_sub_f32_e32 v26, v48, v26
	v_sub_f32_e32 v27, v63, v27
	v_cvt_pk_bf16_f32 v37, v26, v27
	v_lshl_add_u64 v[26:27], s[44:45], 0, v[146:147]
	v_add_co_u32_e32 v48, vcc, 0x13f16000, v26
	s_nop 1
	v_addc_co_u32_e32 v49, vcc, 0, v27, vcc
	global_store_dwordx2 v[48:49], v[44:45], off offset:256
	v_add_co_u32_e32 v44, vcc, 0x1c316000, v26
	s_nop 1
	v_addc_co_u32_e32 v45, vcc, 0, v27, vcc
	global_store_dwordx2 v[44:45], v[46:47], off offset:256
	s_cbranch_scc1 .LBB0_927
	v_lshl_add_u64 v[44:45], s[46:47], 0, v[146:147]
	v_add_co_u32_e32 v46, vcc, 0x13f16000, v44
	s_nop 1
	v_addc_co_u32_e32 v47, vcc, 0, v45, vcc
	global_store_dwordx2 v[46:47], v[28:29], off offset:256
	v_add_co_u32_e32 v28, vcc, 0x1c316000, v44
	s_nop 1
	v_addc_co_u32_e32 v29, vcc, 0, v45, vcc
	global_store_dwordx2 v[28:29], v[36:37], off offset:256
.LBB0_927:
	v_mul_f32_e32 v22, v22, v42
	v_mul_f32_e32 v18, v18, v41
	s_waitcnt vmcnt(12)
	v_mul_f32_e32 v22, v22, v68
	v_mul_f32_e32 v18, v18, v68
	v_add_f32_e32 v28, 1.0, v76
	v_fma_f32 v28, v22, v28, v72
	v_add_f32_e32 v22, 1.0, v84
	v_fma_f32 v29, v18, v22, v80
	v_mul_f32_e32 v18, v23, v42
	v_mul_f32_e32 v18, v18, v69
	v_add_f32_e32 v22, 1.0, v77
	v_fma_f32 v36, v18, v22, v73
	v_mul_f32_e32 v18, v19, v41
	v_mul_f32_e32 v18, v18, v69
	v_add_f32_e32 v19, 1.0, v85
	v_fma_f32 v37, v18, v19, v81
	v_mul_f32_e32 v18, v24, v42
	v_mul_f32_e32 v18, v18, v70
	v_add_f32_e32 v19, 1.0, v78
	v_fma_f32 v43, v18, v19, v74
	v_mul_f32_e32 v18, v20, v41
	v_mul_f32_e32 v18, v18, v70
	v_add_f32_e32 v19, 1.0, v86
	v_fma_f32 v44, v18, v19, v82
	v_mul_f32_e32 v18, v25, v42
	v_mul_f32_e32 v18, v18, v71
	v_add_f32_e32 v19, 1.0, v79
	v_fmac_f32_e32 v75, v18, v19
	v_mul_f32_e32 v18, v21, v41
	v_cvt_pk_bf16_f32 v22, v28, v36
	v_mul_f32_e32 v18, v18, v71
	v_lshlrev_b32_e32 v20, 16, v22
	v_and_b32_e32 v21, 0xffff0000, v22
	v_add_f32_e32 v19, 1.0, v87
	v_sub_f32_e32 v20, v28, v20
	v_sub_f32_e32 v21, v36, v21
	v_fmac_f32_e32 v83, v18, v19
	v_cvt_pk_bf16_f32 v23, v43, v75
	v_cvt_pk_bf16_f32 v18, v29, v37
	v_cvt_pk_bf16_f32 v19, v44, v83
	v_cvt_pk_bf16_f32 v24, v20, v21
	s_nop 0
	v_lshlrev_b32_e32 v20, 16, v23
	v_and_b32_e32 v21, 0xffff0000, v23
	v_sub_f32_e32 v20, v43, v20
	v_sub_f32_e32 v21, v75, v21
	v_cvt_pk_bf16_f32 v25, v20, v21
	v_lshlrev_b32_e32 v20, 16, v18
	v_and_b32_e32 v21, 0xffff0000, v18
	v_sub_f32_e32 v20, v29, v20
	v_sub_f32_e32 v21, v37, v21
	v_cvt_pk_bf16_f32 v20, v20, v21
	v_lshlrev_b32_e32 v21, 16, v19
	v_and_b32_e32 v28, 0xffff0000, v19
	v_sub_f32_e32 v21, v44, v21
	v_sub_f32_e32 v28, v83, v28
	v_cvt_pk_bf16_f32 v21, v21, v28
	v_add_co_u32_e32 v28, vcc, 0x13f16000, v26
	s_nop 1
	v_addc_co_u32_e32 v29, vcc, 0, v27, vcc
	global_store_dwordx2 v[28:29], v[22:23], off offset:768
	v_add_co_u32_e32 v22, vcc, 0x1c316000, v26
	s_nop 1
	v_addc_co_u32_e32 v23, vcc, 0, v27, vcc
	global_store_dwordx2 v[22:23], v[24:25], off offset:768
	v_cndmask_b32_e64 v22, 0, 1, s[28:29]
	v_cmp_ne_u32_e64 s[42:43], 1, v22
	s_andn2_b64 vcc, exec, s[28:29]
	s_cbranch_vccnz .LBB0_929
	v_lshl_add_u64 v[22:23], s[46:47], 0, v[146:147]
	v_add_co_u32_e32 v24, vcc, 0x13f16000, v22
	s_nop 1
	v_addc_co_u32_e32 v25, vcc, 0, v23, vcc
	global_store_dwordx2 v[24:25], v[18:19], off offset:768
	v_add_co_u32_e32 v18, vcc, 0x1c316000, v22
	s_nop 1
	v_addc_co_u32_e32 v19, vcc, 0, v23, vcc
	global_store_dwordx2 v[18:19], v[20:21], off offset:768
; __device__ __forceinline__ unsigned cvt_pk_bf16(float lo, float hi) { unsigned r; asm volatile("v_cvt_pk_bf16_f32 %0, %1, %2" : "=v"(r) : "v"(lo), "v"(hi)); return r; }
; __device__ __forceinline__ float bf_lo(unsigned w) { return __uint_as_float(w << 16); }
; __device__ __forceinline__ float bf_hi(unsigned w) { return __uint_as_float(w & 0xffff0000u); }
;     __device__ __forceinline__ bf16_t* H() const { return (bf16_t*)(ws + WS_H); }
; __device__ __forceinline__ void phase_norm2_route(const Frame& F, const Params& P, int l, int nrows, long long dctx) {
;     ...
;         for (int j = 0; j < 4; ++j) {
;             const int col = F.lane * 4 + 256 * j;
;             const f32x4 gg = *(const f32x4*)(g + col);
;             const f32x4 sha = *(const f32x4*)(mda + 3 * 1024 + col), sca = *(const f32x4*)(mda + 4 * 1024 + col);
;             const f32x4 shb = *(const f32x4*)(mdb + 3 * 1024 + col), scb = *(const f32x4*)(mdb + 4 * 1024 + col);
;             float oa[4], ob[4];
; #pragma unroll
;             for (int i = 0; i < 4; ++i) { oa[i] = va[j][i] * ra * gg[i] * (1.f + sca[i]) + sha[i]; ob[i] = vb[j][i] * rb * gg[i] * (1.f + scb[i]) + shb[i]; }
;             u32x2 ha, hb, la, lb;
;             ha.x = cvt_pk_bf16(oa[0], oa[1]); ha.y = cvt_pk_bf16(oa[2], oa[3]); hb.x = cvt_pk_bf16(ob[0], ob[1]); hb.y = cvt_pk_bf16(ob[2], ob[3]);
;             la.x = cvt_pk_bf16(oa[0] - bf_lo(ha.x), oa[1] - bf_hi(ha.x)); la.y = cvt_pk_bf16(oa[2] - bf_lo(ha.y), oa[3] - bf_hi(ha.y));
;             lb.x = cvt_pk_bf16(ob[0] - bf_lo(hb.x), ob[1] - bf_hi(hb.x)); lb.y = cvt_pk_bf16(ob[2] - bf_lo(hb.y), ob[3] - bf_hi(hb.y));
;             *(u32x2*)(F.H() + (size_t)rowA * DM + col) = ha; *(u32x2*)(LO + (size_t)rowA * DM + col) = la;
;             if (hasB) { *(u32x2*)(F.H() + (size_t)rowB * DM + col) = hb; *(u32x2*)(LO + (size_t)rowB * DM + col) = lb; }
;         }
.LBB0_929:
	s_nop 0
	v_mul_f32_e32 v14, v14, v42
	v_mul_f32_e32 v10, v10, v41
	s_waitcnt vmcnt(9)
	v_mul_f32_e32 v14, v14, v88
	v_mul_f32_e32 v10, v10, v88
	v_add_f32_e32 v28, 1.0, v96
	v_fma_f32 v22, v14, v28, v92
	v_add_f32_e32 v14, 1.0, v104
	v_fma_f32 v18, v10, v14, v100
	v_mul_f32_e32 v10, v15, v42
	v_mul_f32_e32 v10, v10, v89
	v_add_f32_e32 v14, 1.0, v97
	v_fma_f32 v23, v10, v14, v93
	v_mul_f32_e32 v10, v11, v41
	v_mul_f32_e32 v10, v10, v89
	v_add_f32_e32 v11, 1.0, v105
	v_fma_f32 v19, v10, v11, v101
	v_mul_f32_e32 v10, v16, v42
	v_mul_f32_e32 v10, v10, v90
	v_add_f32_e32 v11, 1.0, v98
	v_fma_f32 v24, v10, v11, v94
	v_mul_f32_e32 v10, v12, v41
	v_mul_f32_e32 v10, v10, v90
	v_add_f32_e32 v11, 1.0, v106
	v_fma_f32 v20, v10, v11, v102
	v_mul_f32_e32 v10, v17, v42
	v_mul_f32_e32 v10, v10, v91
	v_add_f32_e32 v11, 1.0, v99
	v_fmac_f32_e32 v95, v10, v11
	v_mul_f32_e32 v10, v13, v41
	v_cvt_pk_bf16_f32 v14, v22, v23
	v_mul_f32_e32 v10, v10, v91
	v_lshlrev_b32_e32 v12, 16, v14
	v_and_b32_e32 v13, 0xffff0000, v14
	v_add_f32_e32 v11, 1.0, v107
	v_sub_f32_e32 v12, v22, v12
	v_sub_f32_e32 v13, v23, v13
	v_fmac_f32_e32 v103, v10, v11
	v_cvt_pk_bf16_f32 v15, v24, v95
	v_cvt_pk_bf16_f32 v10, v18, v19
	v_cvt_pk_bf16_f32 v11, v20, v103
	v_cvt_pk_bf16_f32 v16, v12, v13
	s_nop 0
	v_lshlrev_b32_e32 v12, 16, v15
	v_and_b32_e32 v13, 0xffff0000, v15
	v_sub_f32_e32 v12, v24, v12
	v_sub_f32_e32 v13, v95, v13
	v_cvt_pk_bf16_f32 v17, v12, v13
	v_lshlrev_b32_e32 v12, 16, v10
	v_and_b32_e32 v13, 0xffff0000, v10
	v_sub_f32_e32 v12, v18, v12
	v_sub_f32_e32 v13, v19, v13
	v_cvt_pk_bf16_f32 v12, v12, v13
	v_lshlrev_b32_e32 v13, 16, v11
	v_and_b32_e32 v18, 0xffff0000, v11
	v_sub_f32_e32 v13, v20, v13
	v_sub_f32_e32 v18, v103, v18
	v_cvt_pk_bf16_f32 v13, v13, v18
	v_add_co_u32_e32 v18, vcc, 0x13f16000, v26
	s_nop 1
	v_addc_co_u32_e32 v19, vcc, 0, v27, vcc
	global_store_dwordx2 v[18:19], v[14:15], off offset:1280
	v_add_co_u32_e32 v14, vcc, 0x1c316000, v26
	s_nop 1
	v_addc_co_u32_e32 v15, vcc, 0, v27, vcc
	s_and_b64 vcc, exec, s[42:43]
	global_store_dwordx2 v[14:15], v[16:17], off offset:1280
	s_cbranch_vccnz .LBB0_931
	v_lshl_add_u64 v[14:15], s[46:47], 0, v[146:147]
	v_add_co_u32_e32 v16, vcc, 0x13f16000, v14
	s_nop 1
	v_addc_co_u32_e32 v17, vcc, 0, v15, vcc
	global_store_dwordx2 v[16:17], v[10:11], off offset:1280
	v_add_co_u32_e32 v10, vcc, 0x1c316000, v14
	s_nop 1
	v_addc_co_u32_e32 v11, vcc, 0, v15, vcc
	global_store_dwordx2 v[10:11], v[12:13], off offset:1280
.LBB0_931:
	s_nop 0
	v_mul_f32_e32 v28, v6, v41
	v_add_co_u32_e32 v6, vcc, 0x13f16000, v26
	v_mul_f32_e32 v2, v2, v42
	v_mul_f32_e32 v3, v3, v42
	v_mul_f32_e32 v29, v7, v41
	v_mul_f32_e32 v4, v4, v42
	v_mul_f32_e32 v5, v5, v42
	v_mul_f32_e32 v37, v9, v41
	v_addc_co_u32_e32 v7, vcc, 0, v27, vcc
	v_mul_f32_e32 v36, v8, v41
	v_add_co_u32_e32 v8, vcc, 0x1c316000, v26
	s_waitcnt vmcnt(6)
	v_mul_f32_e32 v2, v2, v108
	v_add_f32_e32 v14, 1.0, v112
	v_mul_f32_e32 v10, v28, v108
	v_add_f32_e32 v18, 1.0, v116
	v_mul_f32_e32 v3, v3, v109
	v_add_f32_e32 v15, 1.0, v113
	v_mul_f32_e32 v11, v29, v109
	v_add_f32_e32 v19, 1.0, v117
	v_mul_f32_e32 v4, v4, v110
	v_add_f32_e32 v16, 1.0, v114
	v_mul_f32_e32 v5, v5, v111
	v_add_f32_e32 v17, 1.0, v115
	v_mul_f32_e32 v13, v37, v111
	v_add_f32_e32 v21, 1.0, v119
	v_addc_co_u32_e32 v9, vcc, 0, v27, vcc
	v_mul_f32_e32 v12, v36, v110
	v_add_f32_e32 v20, 1.0, v118
	v_fma_f32 v14, v2, v14, v120
	v_fma_f32 v18, v10, v18, v124
	v_fma_f32 v15, v3, v15, v121
	v_fma_f32 v19, v11, v19, v125
	v_fma_f32 v4, v4, v16, v122
	v_fmac_f32_e32 v123, v5, v17
	v_fmac_f32_e32 v127, v13, v21
	v_cvt_pk_bf16_f32 v10, v14, v15
	v_cvt_pk_bf16_f32 v11, v4, v123
	v_fma_f32 v12, v12, v20, v126
	v_lshlrev_b32_e32 v5, 16, v10
	v_and_b32_e32 v13, 0xffff0000, v10
	v_lshlrev_b32_e32 v16, 16, v11
	v_cvt_pk_bf16_f32 v2, v18, v19
	v_cvt_pk_bf16_f32 v3, v12, v127
	v_and_b32_e32 v17, 0xffff0000, v11
	v_lshlrev_b32_e32 v20, 16, v2
	v_and_b32_e32 v21, 0xffff0000, v2
	v_lshlrev_b32_e32 v22, 16, v3
	v_and_b32_e32 v23, 0xffff0000, v3
	v_sub_f32_e32 v5, v14, v5
	v_sub_f32_e32 v13, v15, v13
	v_sub_f32_e32 v4, v4, v16
	s_and_b64 vcc, exec, s[42:43]
	v_sub_f32_e32 v14, v123, v17
	v_sub_f32_e32 v15, v18, v20
	v_sub_f32_e32 v16, v19, v21
	v_sub_f32_e32 v17, v12, v22
	v_sub_f32_e32 v18, v127, v23
	v_cvt_pk_bf16_f32 v12, v5, v13
	v_cvt_pk_bf16_f32 v13, v4, v14
	v_cvt_pk_bf16_f32 v4, v15, v16
	v_cvt_pk_bf16_f32 v5, v17, v18
	global_store_dwordx2 v[6:7], v[10:11], off offset:1792
	global_store_dwordx2 v[8:9], v[12:13], off offset:1792
	s_cbranch_vccnz .LBB0_924
	v_lshl_add_u64 v[6:7], s[46:47], 0, v[146:147]
	v_add_co_u32_e32 v8, vcc, 0x13f16000, v6
	s_nop 1
	v_addc_co_u32_e32 v9, vcc, 0, v7, vcc
	global_store_dwordx2 v[8:9], v[2:3], off offset:1792
	v_add_co_u32_e32 v2, vcc, 0x1c316000, v6
	s_nop 1
	v_addc_co_u32_e32 v3, vcc, 0, v7, vcc
	global_store_dwordx2 v[2:3], v[4:5], off offset:1792
	s_branch .LBB0_924
